# combine phase: output stores without the nt hint (on top of the gain hoist)
# speedup vs baseline: 1.0033x; 1.0023x over previous
.LBB0_1397:
	s_add_i32 s39, s33, s2
	s_cmpk_lt_i32 s39, 0x4000
	s_cselect_b32 s16, s39, s2
	s_lshl_b32 s18, s16, 2
	s_ashr_i32 s17, s16, 31
	s_ashr_i32 s19, s18, 31
	s_lshl_b64 s[0:1], s[16:17], 11
	s_lshl_b64 s[16:17], s[18:19], 2
	s_add_u32 s22, s40, s16
	s_addc_u32 s23, s41, s17
	s_add_u32 s20, s44, s16
	s_addc_u32 s21, s45, s17
	s_add_u32 s16, s36, s16
	s_addc_u32 s17, s37, s17
	s_or_b32 s18, s18, 2
	s_ashr_i32 s19, s18, 31
	s_lshl_b64 s[18:19], s[18:19], 2
	s_add_u32 s18, s36, s18
	s_addc_u32 s19, s37, s19
	s_ashr_i32 s15, s14, 31
	global_load_dwordx4 v[0:3], v9, s[22:23]
	s_add_i32 s30, s14, -3
	s_lshl_b64 s[22:23], s[14:15], 2
	s_add_u32 s34, s44, s22
	s_addc_u32 s35, s45, s23
	s_add_u32 s26, s40, s22
	s_addc_u32 s27, s41, s23
	s_add_i32 s24, s14, -1
	s_ashr_i32 s25, s24, 31
	s_lshl_b64 s[24:25], s[24:25], 2
	s_add_u32 s42, s44, s24
	s_addc_u32 s43, s45, s25
	s_add_u32 s28, s40, s24
	s_addc_u32 s29, s41, s25
	global_load_dword v19, v9, s[26:27]
	global_load_dword v25, v9, s[28:29]
	s_add_i32 s26, s14, -2
	s_ashr_i32 s27, s26, 31
	s_lshl_b64 s[26:27], s[26:27], 2
	s_add_u32 s28, s44, s26
	s_addc_u32 s29, s45, s27
	s_add_u32 s46, s40, s26
	s_addc_u32 s47, s41, s27
	global_load_dword v38, v9, s[46:47]
	global_load_dword v39, v9, s[42:43]
	global_load_dword v40, v9, s[34:35]
	s_ashr_i32 s31, s30, 31
	s_lshl_b64 s[30:31], s[30:31], 2
	s_add_u32 s34, s44, s30
	s_addc_u32 s35, s45, s31
	s_add_u32 s42, s40, s30
	s_addc_u32 s43, s41, s31
	global_load_dword v41, v9, s[42:43]
	global_load_dword v42, v9, s[28:29]
	global_load_dword v43, v9, s[34:35]
	global_load_dwordx2 v[26:27], v[16:17], off offset:1536 nt
	global_load_dwordx2 v[36:37], v[16:17], off offset:1024 nt
	global_load_dwordx2 v[20:21], v[16:17], off offset:512 nt
	global_load_dwordx4 v[4:7], v9, s[20:21]
	s_add_u32 s20, s36, s22
	s_addc_u32 s21, s37, s23
	s_add_u32 s22, s36, s24
	s_addc_u32 s23, s37, s25
	global_load_dword v18, v9, s[20:21]
	s_add_u32 s20, s36, s26
	s_addc_u32 s21, s37, s27
	s_add_u32 s24, s36, s30
	s_addc_u32 s25, s37, s31
	global_load_dword v24, v9, s[22:23]
	global_load_dword v22, v9, s[20:21]
	global_load_dword v23, v9, s[24:25]
	s_cmpk_gt_i32 s39, 0x3fff
	s_waitcnt vmcnt(0)
	v_lshlrev_b32_e32 v1, 2, v1
	v_lshlrev_b32_e32 v2, 2, v2
	v_lshlrev_b32_e32 v3, 2, v3
	v_add_u32_e32 v1, s5, v1
	v_add_u32_e32 v2, s5, v2
	v_add_u32_e32 v3, s5, v3
	v_lshlrev_b32_e32 v0, 2, v0
	v_add_u32_e32 v0, s5, v0
	v_lshlrev_b32_e32 v19, 2, v19
	v_lshlrev_b32_e32 v25, 2, v25
	v_add_u32_e32 v19, s5, v19
	v_add_u32_e32 v25, s5, v25
	v_lshlrev_b32_e32 v38, 2, v38
	v_add_u32_e32 v38, s5, v38
	ds_read_b32 v1, v1
	ds_read_b32 v25, v25
	ds_read_b32 v114, v2
	ds_read_b32 v115, v3
	ds_read_b32 v19, v19
	ds_read_b32 v44, v38
	s_waitcnt lgkmcnt(0)
	v_add_u32_e32 v2, v39, v25
	v_ashrrev_i32_e32 v3, 31, v2
	v_lshlrev_b64 v[2:3], 10, v[2:3]
	v_lshl_add_u64 v[38:39], v[14:15], 0, v[2:3]
	global_load_dword v60, v[38:39], off offset:768 nt
	global_load_dword v48, v[38:39], off nt
	global_load_dword v56, v[38:39], off offset:512 nt
	global_load_dword v52, v[38:39], off offset:256 nt
	global_load_dwordx2 v[2:3], v9, s[18:19]
	v_add_u32_e32 v38, v40, v19
	v_ashrrev_i32_e32 v39, 31, v38
	v_lshlrev_b64 v[38:39], 10, v[38:39]
	v_lshlrev_b32_e32 v19, 2, v41
	v_lshl_add_u64 v[38:39], v[14:15], 0, v[38:39]
	v_add_u32_e32 v19, s5, v19
	global_load_dword v64, v[38:39], off nt
	global_load_dword v68, v[38:39], off offset:256 nt
	global_load_dword v72, v[38:39], off offset:512 nt
	ds_read_b32 v19, v19
	v_add_u32_e32 v40, v42, v44
	v_ashrrev_i32_e32 v41, 31, v40
	v_lshlrev_b64 v[40:41], 10, v[40:41]
	v_lshl_add_u64 v[40:41], v[14:15], 0, v[40:41]
	s_waitcnt lgkmcnt(0)
	v_add_u32_e32 v42, v43, v19
	v_ashrrev_i32_e32 v43, 31, v42
	v_lshlrev_b64 v[42:43], 10, v[42:43]
	global_load_dword v74, v[40:41], off offset:768 nt
	v_lshl_add_u64 v[42:43], v[14:15], 0, v[42:43]
	global_load_dword v86, v[42:43], off nt
	global_load_dword v90, v[42:43], off offset:256 nt
	global_load_dword v94, v[42:43], off offset:512 nt
	global_load_dword v98, v[42:43], off offset:768 nt
	global_load_dword v102, v[40:41], off nt
	global_load_dword v106, v[40:41], off offset:256 nt
	global_load_dword v110, v[40:41], off offset:512 nt
	global_load_dword v116, v[38:39], off offset:768 nt
	global_load_dwordx2 v[44:45], v[16:17], off nt
	v_lshlrev_b32_e32 v40, 16, v36
	v_lshlrev_b32_e32 v119, 16, v20
	v_and_b32_e32 v20, 0xffff0000, v20
	v_lshlrev_b32_e32 v38, 16, v26
	v_lshlrev_b32_e32 v42, 16, v37
	v_mov_b32_e32 v25, v22
	v_and_b32_e32 v117, 0xffff0000, v36
	v_mov_b32_e32 v19, v24
	v_and_b32_e32 v39, 0xffff0000, v26
	v_lshlrev_b32_e32 v41, 16, v27
	v_and_b32_e32 v43, 0xffff0000, v27
	v_mov_b32_e32 v27, v22
	v_mov_b32_e32 v26, v23
	v_and_b32_e32 v118, 0xffff0000, v37
	v_mov_b32_e32 v37, v18
	v_mov_b32_e32 v36, v24
	s_waitcnt vmcnt(17)
	v_cvt_pk_f32_fp8_e32 v[58:59], v60
	s_waitcnt vmcnt(16)
	v_cvt_pk_f32_fp8_e32 v[46:47], v48
	s_waitcnt vmcnt(15)
	v_cvt_pk_f32_fp8_e32 v[54:55], v56
	s_waitcnt vmcnt(14)
	v_cvt_pk_f32_fp8_e32 v[50:51], v52
	v_cvt_pk_f32_fp8_sdwa v[52:53], v52 src0_sel:WORD_1
	v_mul_f32_e32 v75, v24, v59
	v_cvt_pk_f32_fp8_sdwa v[56:57], v56 src0_sel:WORD_1
	v_mov_b32_e32 v77, v51
	v_mov_b32_e32 v78, v52
	s_waitcnt vmcnt(12)
	v_cvt_pk_f32_fp8_e32 v[62:63], v64
	s_waitcnt vmcnt(11)
	v_cvt_pk_f32_fp8_e32 v[66:67], v68
	v_cvt_pk_f32_fp8_sdwa v[68:69], v68 src0_sel:WORD_1
	s_waitcnt vmcnt(10)
	v_cvt_pk_f32_fp8_e32 v[70:71], v72
	v_cvt_pk_f32_fp8_sdwa v[72:73], v72 src0_sel:WORD_1
	s_waitcnt vmcnt(8)
	v_cvt_pk_f32_fp8_e32 v[84:85], v86
	s_waitcnt vmcnt(7)
	v_cvt_pk_f32_fp8_e32 v[88:89], v90
	s_waitcnt vmcnt(6)
	v_cvt_pk_f32_fp8_e32 v[92:93], v94
	v_cvt_pk_f32_fp8_sdwa v[90:91], v90 src0_sel:WORD_1
	v_cvt_pk_f32_fp8_sdwa v[94:95], v94 src0_sel:WORD_1
	s_waitcnt vmcnt(3)
	v_cvt_pk_f32_fp8_e32 v[104:105], v106
	v_cvt_pk_f32_fp8_e32 v[80:81], v74
	s_waitcnt vmcnt(2)
	v_cvt_pk_f32_fp8_e32 v[108:109], v110
	v_cvt_pk_f32_fp8_e32 v[96:97], v98
	v_mov_b32_e32 v113, v88
	v_mov_b32_e32 v88, v105
	v_cvt_pk_f32_fp8_e32 v[100:101], v102
	v_cvt_pk_f32_fp8_sdwa v[106:107], v106 src0_sel:WORD_1
	v_cvt_pk_f32_fp8_sdwa v[110:111], v110 src0_sel:WORD_1
	v_pk_mul_f32 v[88:89], v[22:23], v[88:89]
	v_mov_b32_e32 v59, v80
	v_fmac_f32_e32 v40, v23, v92
	v_mov_b32_e32 v112, v104
	v_mov_b32_e32 v92, v109
	v_add_f32_e32 v20, v89, v20
	v_pk_mul_f32 v[58:59], v[24:25], v[58:59]
	v_fmac_f32_e32 v42, v23, v94
	v_fmac_f32_e32 v38, v23, v96
	v_mov_b32_e32 v104, v90
	v_mov_b32_e32 v90, v95
	v_pk_mul_f32 v[94:95], v[22:23], v[112:113]
	v_pk_mul_f32 v[92:93], v[22:23], v[92:93]
	v_add_f32_e32 v20, v88, v20
	s_waitcnt vmcnt(0)
	v_lshlrev_b32_e32 v88, 16, v44
	v_and_b32_e32 v89, 0xffff0000, v44
	v_mov_b32_e32 v44, v23
	v_mov_b32_e32 v79, v68
	v_mov_b32_e32 v68, v53
	v_mov_b32_e32 v52, v71
	v_mov_b32_e32 v53, v55
	v_cvt_pk_f32_fp8_sdwa v[86:87], v86 src0_sel:WORD_1
	v_cvt_pk_f32_fp8_sdwa v[98:99], v98 src0_sel:WORD_1
	v_add_f32_e32 v38, v59, v38
	v_add_f32_e32 v51, v95, v119
	v_add_f32_e32 v55, v93, v117
	v_pk_fma_f32 v[84:85], v[44:45], v[84:85], v[88:89] op_sel_hi:[0,1,1]
	v_cvt_pk_f32_fp8_sdwa v[82:83], v74 src0_sel:WORD_1
	v_pk_mul_f32 v[52:53], v[18:19], v[52:53]
	v_cvt_pk_f32_fp8_sdwa v[102:103], v102 src0_sel:WORD_1
	v_mov_b32_e32 v105, v106
	v_mov_b32_e32 v106, v91
	v_mov_b32_e32 v91, v111
	v_add_f32_e32 v59, v58, v38
	v_add_f32_e32 v38, v94, v51
	v_add_f32_e32 v51, v92, v55
	v_pk_fma_f32 v[84:85], v[22:23], v[100:101], v[84:85] op_sel_hi:[0,1,1]
	v_cvt_pk_f32_fp8_sdwa v[48:49], v48 src0_sel:WORD_1
	v_mov_b32_e32 v76, v67
	v_pk_mul_f32 v[104:105], v[26:27], v[104:105]
	v_pk_mul_f32 v[106:107], v[26:27], v[106:107]
	v_pk_mul_f32 v[26:27], v[26:27], v[90:91]
	v_add_f32_e32 v51, v53, v51
	v_pk_fma_f32 v[46:47], v[24:25], v[46:47], v[84:85] op_sel_hi:[0,1,1]
	v_cvt_pk_f32_fp8_sdwa v[60:61], v60 src0_sel:WORD_1
	v_pk_mul_f32 v[76:77], v[18:19], v[76:77]
	v_add_f32_e32 v26, v26, v118
	v_add_f32_e32 v80, v52, v51
	v_mov_b32_e32 v52, v57
	v_mov_b32_e32 v53, v73
	v_pk_fma_f32 v[62:63], v[18:19], v[62:63], v[46:47] op_sel_hi:[0,1,1]
	v_lshlrev_b32_e32 v46, 16, v45
	v_and_b32_e32 v47, 0xffff0000, v45
	v_pk_mul_f32 v[78:79], v[36:37], v[78:79]
	v_pk_mul_f32 v[68:69], v[36:37], v[68:69]
	v_add_f32_e32 v27, v26, v27
	v_add_f32_e32 v20, v77, v20
	v_pk_mul_f32 v[36:37], v[36:37], v[52:53]
	v_pk_fma_f32 v[44:45], v[44:45], v[86:87], v[46:47] op_sel_hi:[0,1,1]
	v_mov_b32_e32 v109, v98
	v_mov_b32_e32 v111, v99
	v_add_f32_e32 v26, v76, v20
	v_cvt_pk_f32_fp8_sdwa v[52:53], v116 src0_sel:WORD_1
	v_add_f32_e32 v20, v27, v36
	v_pk_fma_f32 v[44:45], v[22:23], v[102:103], v[44:45] op_sel_hi:[0,1,1]
	v_pk_fma_f32 v[40:41], v[22:23], v[108:109], v[40:41]
	v_pk_fma_f32 v[42:43], v[22:23], v[110:111], v[42:43]
	v_mov_b32_e32 v46, v24
	v_mov_b32_e32 v47, v23
	v_mov_b32_e32 v51, v97
	v_mov_b32_e32 v55, v82
	v_mov_b32_e32 v57, v83
	v_add_f32_e32 v90, v20, v37
	v_cvt_pk_f32_fp8_e32 v[36:37], v116
	v_pk_fma_f32 v[44:45], v[24:25], v[48:49], v[44:45] op_sel_hi:[0,1,1]
	v_pk_fma_f32 v[38:39], v[46:47], v[50:51], v[38:39]
	v_pk_fma_f32 v[40:41], v[24:25], v[54:55], v[40:41]
	v_pk_fma_f32 v[24:25], v[24:25], v[56:57], v[42:43]
	v_mov_b32_e32 v42, v18
	v_mov_b32_e32 v43, v22
	v_mov_b32_e32 v67, v81
	v_pk_fma_f32 v[54:55], v[42:43], v[66:67], v[38:39]
	v_mov_b32_e32 v71, v60
	v_pk_fma_f32 v[56:57], v[18:19], v[70:71], v[40:41]
	v_mov_b32_e32 v73, v61
	v_mov_b32_e32 v74, v54
	v_cvt_pk_f32_fp8_sdwa v[64:65], v64 src0_sel:WORD_1
	v_mul_f32_e32 v77, v18, v52
	v_pk_fma_f32 v[60:61], v[18:19], v[72:73], v[24:25]
	v_pk_mul_f32 v[22:23], v[54:55], v[54:55]
	v_pk_add_f32 v[24:25], v[54:55], v[74:75]
	v_mov_b32_e32 v76, v56
	v_mul_f32_e32 v53, v18, v53
	v_mul_f32_e32 v20, v80, v80
	v_mov_b32_e32 v23, v25
	v_mov_b32_e32 v27, v18
	v_mov_b32_e32 v38, v26
	v_mov_b32_e32 v39, v37
	v_pk_add_f32 v[48:49], v[56:57], v[76:77]
	v_mov_b32_e32 v52, v60
	v_mul_f32_e32 v58, v90, v90
	v_pk_fma_f32 v[66:67], v[26:27], v[38:39], v[22:23]
	v_pk_add_f32 v[70:71], v[60:61], v[52:53]
	v_pk_fma_f32 v[22:23], v[56:57], v[56:57], v[20:21]
	v_pk_mul_f32 v[38:39], v[48:49], v[48:49]
	v_pk_mul_f32 v[40:41], v[70:71], v[70:71]
	v_mov_b32_e32 v23, v39
	v_pk_fma_f32 v[38:39], v[60:61], v[60:61], v[58:59]
	v_pk_fma_f32 v[64:65], v[18:19], v[64:65], v[44:45] op_sel_hi:[0,1,1]
	v_mov_b32_e32 v39, v41
	v_pk_mul_f32 v[44:45], v[64:65], v[64:65]
	v_pk_add_f32 v[22:23], v[22:23], v[38:39]
	v_mov_b32_e32 v38, v62
	v_mov_b32_e32 v39, v18
	v_mov_b32_e32 v40, v62
	v_mov_b32_e32 v41, v36
	v_mul_f32_e32 v58, v63, v63
	v_mov_b32_e32 v42, v64
	v_mov_b32_e32 v43, v18
	v_mov_b32_e32 v46, v64
	v_mov_b32_e32 v47, v36
	v_pk_fma_f32 v[72:73], v[38:39], v[40:41], v[58:59]
	v_mov_b32_e32 v58, v45
	v_pk_fma_f32 v[38:39], v[42:43], v[46:47], v[58:59]
	v_lshlrev_b32_e32 v20, 16, v21
	v_pk_add_f32 v[40:41], v[72:73], v[38:39]
	v_pk_mul_f32 v[38:39], v[72:73], v[38:39]
	v_and_b32_e32 v21, 0xffff0000, v21
	v_mov_b32_e32 v41, v39
	v_mov_b32_e32 v38, v104
	v_mov_b32_e32 v39, v106
	v_pk_add_f32 v[20:21], v[38:39], v[20:21]
	v_mov_b32_e32 v106, v105
	v_pk_add_f32 v[20:21], v[20:21], v[106:107]
	v_mov_b32_e32 v38, v78
	v_mov_b32_e32 v39, v68
	v_pk_add_f32 v[20:21], v[20:21], v[38:39]
	v_mov_b32_e32 v68, v79
	v_pk_add_f32 v[58:59], v[20:21], v[68:69]
	v_lshl_add_u64 v[38:39], v[12:13], 0, s[0:1]
	v_pk_mul_f32 v[20:21], v[58:59], v[58:59]
	v_pk_mov_b32 v[18:19], v[58:59], v[18:19] op_sel:[1,0]
	v_mov_b32_e32 v36, v59
	v_mov_b32_e32 v21, v25
	v_pk_fma_f32 v[18:19], v[18:19], v[36:37], v[20:21]
	s_nop 0
	v_pk_add_f32 v[20:21], v[66:67], v[18:19]
	v_pk_mul_f32 v[18:19], v[66:67], v[18:19]
	s_nop 0
	v_mov_b32_e32 v21, v19
	v_pk_add_f32 v[18:19], v[40:41], v[20:21]
	s_nop 0
	v_pk_add_f32 v[18:19], v[18:19], v[22:23]
	ds_read_b32 v22, v0
	v_add_f32_e32 v18, v18, v19
	ds_bpermute_b32 v19, v28, v18
	v_add_u32_e32 v0, v5, v1
	v_ashrrev_i32_e32 v1, 31, v0
	s_waitcnt lgkmcnt(1)
	v_add_u32_e32 v4, v4, v22
	v_ashrrev_i32_e32 v5, 31, v4
	s_waitcnt lgkmcnt(0)
	v_add_f32_e32 v23, v18, v19
	global_load_dwordx2 v[20:21], v9, s[16:17]
	global_load_dwordx2 v[18:19], v9, s[16:17] offset:4
	ds_bpermute_b32 v24, v29, v23
	v_lshlrev_b64 v[36:37], 10, v[4:5]
	v_add_u32_e32 v4, v6, v114
	v_ashrrev_i32_e32 v5, 31, v4
	v_lshlrev_b64 v[68:69], 10, v[4:5]
	s_waitcnt lgkmcnt(0)
	v_add_f32_e32 v23, v23, v24
	ds_bpermute_b32 v27, v30, v23
	v_lshlrev_b64 v[24:25], 10, v[0:1]
	v_add_u32_e32 v0, v7, v115
	v_lshl_add_u64 v[36:37], v[14:15], 0, v[36:37]
	v_lshl_add_u64 v[24:25], v[14:15], 0, v[24:25]
	s_waitcnt lgkmcnt(0)
	v_add_f32_e32 v1, v23, v27
	ds_bpermute_b32 v22, v31, v1
	v_lshl_add_u64 v[68:69], v[14:15], 0, v[68:69]
	s_waitcnt lgkmcnt(0)
	v_add_f32_e32 v6, v1, v22
	ds_bpermute_b32 v7, v32, v6
	v_ashrrev_i32_e32 v1, 31, v0
	v_lshlrev_b64 v[40:41], 10, v[0:1]
	v_lshl_add_u64 v[74:75], v[14:15], 0, v[40:41]
	s_waitcnt lgkmcnt(0)
	v_add_f32_e32 v27, v6, v7
	ds_bpermute_b32 v42, v33, v27
	global_load_dwordx2 v[4:5], v[38:39], off nt
	global_load_dwordx2 v[0:1], v[38:39], off offset:512 nt
	global_load_dwordx2 v[6:7], v[38:39], off offset:1024 nt
	global_load_dwordx2 v[22:23], v[38:39], off offset:1536 nt
	s_waitcnt lgkmcnt(0)
	v_add_f32_e32 v27, v27, v42
	v_fmamk_f32 v27, v27, 0x3a800000, v34
	v_mul_f32_e32 v38, 0x4f800000, v27
	v_cmp_gt_f32_e32 vcc, s38, v27
	s_nop 1
	v_cndmask_b32_e32 v39, v27, v38, vcc
	v_sqrt_f32_e32 v42, v39
	global_load_dword v48, v[36:37], off nt
	global_load_dword v46, v[36:37], off offset:256 nt
	global_load_dword v47, v[36:37], off offset:512 nt
	global_load_dword v45, v[36:37], off offset:768 nt
	global_load_dword v44, v[24:25], off nt
	global_load_dword v43, v[24:25], off offset:256 nt
	global_load_dword v38, v[24:25], off offset:512 nt
	global_load_dword v27, v[24:25], off offset:768 nt
	v_add_u32_e32 v24, -1, v42
	v_fma_f32 v25, -v24, v42, v39
	v_cmp_ge_f32_e64 s[0:1], 0, v25
	v_add_u32_e32 v25, 1, v42
	v_fma_f32 v36, -v25, v42, v39
	v_cndmask_b32_e64 v24, v42, v24, s[0:1]
	v_cmp_lt_f32_e64 s[0:1], 0, v36
	s_nop 1
	v_cndmask_b32_e64 v24, v24, v25, s[0:1]
	v_mul_f32_e32 v25, 0x37800000, v24
	v_cndmask_b32_e32 v24, v24, v25, vcc
	v_cmp_class_f32_e32 vcc, v39, v35
	s_nop 1
	v_cndmask_b32_e32 v55, v24, v39, vcc
	v_div_scale_f32 v57, s[0:1], v55, v55, 1.0
	v_rcp_f32_e32 v61, v57
	global_load_dword v42, v[68:69], off nt
	global_load_dword v41, v[68:69], off offset:256 nt
	global_load_dword v40, v[68:69], off offset:512 nt
	global_load_dword v39, v[68:69], off offset:768 nt
	global_load_dword v36, v[74:75], off nt
	global_load_dword v37, v[74:75], off offset:256 nt
	global_load_dword v25, v[74:75], off offset:512 nt
	global_load_dword v24, v[74:75], off offset:768 nt
	v_lshl_add_u64 v[68:69], s[10:11], 0, v[8:9]
	v_fma_f32 v66, -v57, v61, 1.0
	v_fmac_f32_e32 v61, v66, v61
	v_div_scale_f32 v66, vcc, 1.0, v55, 1.0
	v_mul_f32_e32 v70, v66, v61
	v_fma_f32 v72, -v57, v70, v66
	v_fmac_f32_e32 v70, v72, v61
	v_fma_f32 v57, -v57, v70, v66
	v_div_fmas_f32 v57, v57, v61, v70
	v_div_fixup_f32 v72, v57, v55, 1.0
	v_pk_mul_f32 v[62:63], v[72:73], v[62:63] op_sel_hi:[0,1]
	v_pk_mul_f32 v[64:65], v[72:73], v[64:65] op_sel_hi:[0,1]
	v_mov_b32_e32 v55, v26
	v_pk_mul_f32 v[58:59], v[72:73], v[58:59] op_sel_hi:[0,1]
	v_pk_mul_f32 v[54:55], v[72:73], v[54:55] op_sel_hi:[0,1]
	v_mov_b32_e32 v57, v80
	v_mov_b32_e32 v61, v90
	s_waitcnt vmcnt(20)
	v_pk_mul_f32 v[52:53], v[202:203], v[64:65]
	v_pk_mul_f32 v[50:51], v[200:201], v[62:63]
	global_store_dwordx4 v[68:69], v[50:53], off
	v_pk_mul_f32 v[56:57], v[72:73], v[56:57] op_sel_hi:[0,1]
	v_mov_b32_e32 v70, v49
	v_mov_b32_e32 v66, v73
	v_pk_mul_f32 v[50:51], v[204:205], v[54:55]
	v_pk_mul_f32 v[52:53], v[206:207], v[58:59]
	global_store_dwordx4 v[68:69], v[50:53], off offset:1024
	v_pk_mul_f32 v[54:55], v[72:73], v[60:61] op_sel_hi:[0,1]
	s_nop 1
	v_pk_mul_f32 v[50:51], v[208:209], v[56:57]
	v_pk_mul_f32 v[52:53], v[210:211], v[54:55]
	global_store_dwordx4 v[68:69], v[50:53], off offset:2048
	v_pk_mul_f32 v[54:55], v[72:73], v[66:67] op_sel_hi:[0,1]
	v_pk_mul_f32 v[56:57], v[72:73], v[70:71] op_sel_hi:[0,1]
	v_pk_mul_f32 v[50:51], v[212:213], v[54:55]
	v_pk_mul_f32 v[52:53], v[214:215], v[56:57]
	global_store_dwordx4 v[68:69], v[50:53], off offset:3072
	s_waitcnt vmcnt(4)
	s_cbranch_scc1 .LBB0_1396
	s_nop 0
	v_and_b32_e32 v51, 0xffff0000, v23
	v_lshlrev_b32_e32 v53, 16, v23
	v_and_b32_e32 v49, 0xffff0000, v22
	v_lshlrev_b32_e32 v82, 16, v22
	v_cvt_pk_f32_fp8_e32 v[22:23], v46
	v_cvt_pk_f32_fp8_e32 v[66:67], v43
	v_mov_b32_e32 v70, v18
	v_mov_b32_e32 v71, v20
	v_mov_b32_e32 v73, v22
	v_mov_b32_e32 v72, v66
	v_and_b32_e32 v75, 0xffff0000, v0
	v_lshlrev_b32_e32 v0, 16, v0
	v_cvt_pk_f32_fp8_e32 v[56:57], v47
	v_cvt_pk_f32_fp8_sdwa v[58:59], v47 src0_sel:WORD_1
	v_cvt_pk_f32_fp8_sdwa v[46:47], v46 src0_sel:WORD_1
	v_cvt_pk_f32_fp8_sdwa v[68:69], v43 src0_sel:WORD_1
	v_pk_mul_f32 v[72:73], v[70:71], v[72:73]
	v_mov_b32_e32 v22, v67
	v_add_f32_e32 v0, v73, v0
	v_and_b32_e32 v26, 0xffff0000, v7
	v_lshlrev_b32_e32 v50, 16, v7
	v_and_b32_e32 v74, 0xffff0000, v6
	v_lshlrev_b32_e32 v52, 16, v6
	v_cvt_pk_f32_fp8_e32 v[6:7], v48
	v_cvt_pk_f32_fp8_sdwa v[54:55], v48 src0_sel:WORD_1
	v_add_f32_e32 v48, v72, v0
	v_pk_mul_f32 v[22:23], v[70:71], v[22:23]
	v_cvt_pk_f32_fp8_e32 v[72:73], v38
	v_add_f32_e32 v0, v23, v75
	v_add_f32_e32 v0, v22, v0
	v_mov_b32_e32 v22, v20
	v_mov_b32_e32 v23, v18
	v_mov_b32_e32 v67, v68
	v_mov_b32_e32 v68, v47
	v_cvt_pk_f32_fp8_e32 v[60:61], v45
	v_mov_b32_e32 v66, v46
	v_pk_mul_f32 v[46:47], v[22:23], v[68:69]
	v_cvt_pk_f32_fp8_sdwa v[68:69], v38 src0_sel:WORD_1
	v_fmac_f32_e32 v52, v20, v56
	v_mov_b32_e32 v56, v73
	v_pk_mul_f32 v[56:57], v[70:71], v[56:57]
	v_fmac_f32_e32 v82, v20, v60
	v_add_f32_e32 v38, v57, v74
	v_add_f32_e32 v60, v56, v38
	v_mov_b32_e32 v56, v59
	v_mov_b32_e32 v57, v69
	v_pk_mul_f32 v[66:67], v[22:23], v[66:67]
	v_pk_mul_f32 v[22:23], v[22:23], v[56:57]
	v_cvt_pk_f32_fp8_e32 v[56:57], v27
	v_cvt_pk_f32_fp8_e32 v[76:77], v39
	v_mov_b32_e32 v78, v2
	v_mov_b32_e32 v79, v18
	v_mov_b32_e32 v81, v56
	v_mov_b32_e32 v80, v76
	v_cvt_pk_f32_fp8_e32 v[70:71], v41
	v_pk_mul_f32 v[78:79], v[78:79], v[80:81]
	v_cvt_pk_f32_fp8_e32 v[80:81], v37
	v_add_f32_e32 v22, v22, v26
	v_add_f32_e32 v69, v22, v23
	v_cvt_pk_f32_fp8_sdwa v[22:23], v41 src0_sel:WORD_1
	v_add_f32_e32 v56, v79, v82
	v_cvt_pk_f32_fp8_e32 v[82:83], v36
	v_cvt_pk_f32_fp8_sdwa v[84:85], v36 src0_sel:WORD_1
	v_cvt_pk_f32_fp8_sdwa v[36:37], v37 src0_sel:WORD_1
	v_cvt_pk_f32_fp8_e32 v[74:75], v40
	v_cvt_pk_f32_fp8_e32 v[88:89], v25
	v_mov_b32_e32 v86, v81
	v_mov_b32_e32 v87, v71
	v_pk_mul_f32 v[86:87], v[2:3], v[86:87] op_sel:[1,0] op_sel_hi:[0,1]
	v_cvt_pk_f32_fp8_sdwa v[40:41], v40 src0_sel:WORD_1
	v_add_f32_e32 v0, v87, v0
	v_mov_b32_e32 v87, v22
	v_mov_b32_e32 v22, v37
	v_cvt_pk_f32_fp8_sdwa v[90:91], v25 src0_sel:WORD_1
	v_add_f32_e32 v79, v78, v56
	v_add_f32_e32 v56, v86, v0
	v_mov_b32_e32 v86, v36
	v_pk_mul_f32 v[36:37], v[2:3], v[22:23] op_sel:[1,0] op_sel_hi:[0,1]
	v_mov_b32_e32 v22, v89
	v_mov_b32_e32 v23, v75
	v_cvt_pk_f32_fp8_sdwa v[62:63], v45 src0_sel:WORD_1
	v_pk_mul_f32 v[22:23], v[2:3], v[22:23] op_sel:[1,0] op_sel_hi:[0,1]
	v_cvt_pk_f32_fp8_e32 v[64:65], v44
	v_cvt_pk_f32_fp8_sdwa v[44:45], v44 src0_sel:WORD_1
	v_cvt_pk_f32_fp8_sdwa v[26:27], v27 src0_sel:WORD_1
	v_add_f32_e32 v0, v23, v60
	v_add_f32_e32 v100, v22, v0
	v_mov_b32_e32 v22, v91
	v_mov_b32_e32 v23, v41
	v_pk_mul_f32 v[22:23], v[2:3], v[22:23] op_sel:[1,0] op_sel_hi:[0,1]
	v_lshlrev_b32_e32 v98, 16, v4
	v_and_b32_e32 v99, 0xffff0000, v4
	v_lshlrev_b32_e32 v4, 16, v5
	v_and_b32_e32 v5, 0xffff0000, v5
	v_fmac_f32_e32 v50, v20, v58
	v_add_f32_e32 v0, v69, v23
	v_pk_fma_f32 v[4:5], v[20:21], v[54:55], v[4:5] op_sel_hi:[0,1,1]
	v_mov_b32_e32 v73, v62
	v_mov_b32_e32 v69, v63
	v_cvt_pk_f32_fp8_sdwa v[38:39], v39 src0_sel:WORD_1
	v_pk_fma_f32 v[4:5], v[18:19], v[44:45], v[4:5] op_sel_hi:[0,1,1]
	v_pk_fma_f32 v[44:45], v[20:21], v[72:73], v[52:53] op_sel:[1,0,0] op_sel_hi:[0,1,1]
	v_pk_fma_f32 v[50:51], v[20:21], v[68:69], v[50:51] op_sel:[1,0,0] op_sel_hi:[0,1,1]
	v_mov_b32_e32 v52, v2
	v_mov_b32_e32 v53, v20
	v_mov_b32_e32 v71, v61
	v_mov_b32_e32 v41, v27
	v_cvt_pk_f32_fp8_sdwa v[92:93], v24 src0_sel:WORD_1
	v_cvt_pk_f32_fp8_e32 v[94:95], v24
	v_pk_fma_f32 v[6:7], v[20:21], v[6:7], v[98:99] op_sel_hi:[0,1,1]
	v_pk_fma_f32 v[20:21], v[52:53], v[70:71], v[48:49]
	v_mov_b32_e32 v75, v26
	v_pk_fma_f32 v[26:27], v[18:19], v[40:41], v[50:51] op_sel:[1,0,0] op_sel_hi:[0,1,1]
	v_mov_b32_e32 v40, v3
	v_mov_b32_e32 v41, v18
	v_mov_b32_e32 v81, v57
	v_pk_mul_f32 v[76:77], v[2:3], v[76:77] op_sel:[1,0] op_sel_hi:[0,1]
	v_pk_fma_f32 v[6:7], v[18:19], v[64:65], v[6:7] op_sel_hi:[0,1,1]
	v_pk_fma_f32 v[44:45], v[18:19], v[74:75], v[44:45] op_sel:[1,0,0] op_sel_hi:[0,1,1]
	v_pk_fma_f32 v[18:19], v[40:41], v[80:81], v[20:21]
	v_mov_b32_e32 v89, v38
	v_mov_b32_e32 v76, v18
	v_mov_b32_e32 v91, v39
	v_pk_mul_f32 v[38:39], v[18:19], v[18:19]
	v_pk_add_f32 v[40:41], v[18:19], v[76:77]
	v_cvt_pk_f32_fp8_e32 v[58:59], v42
	v_cvt_pk_f32_fp8_sdwa v[42:43], v42 src0_sel:WORD_1
	v_pk_mul_f32 v[96:97], v[2:3], v[92:93] op_sel:[1,0] op_sel_hi:[0,1]
	v_pk_fma_f32 v[20:21], v[2:3], v[88:89], v[44:45] op_sel:[1,0,0] op_sel_hi:[0,1,1]
	v_mov_b32_e32 v39, v41
	v_mov_b32_e32 v57, v3
	v_mov_b32_e32 v44, v56
	v_mov_b32_e32 v45, v95
	v_pk_mul_f32 v[92:93], v[2:3], v[92:93]
	v_pk_fma_f32 v[26:27], v[2:3], v[90:91], v[26:27] op_sel:[1,0,0] op_sel_hi:[0,1,1]
	v_pk_fma_f32 v[38:39], v[56:57], v[44:45], v[38:39]
	v_mov_b32_e32 v44, v20
	v_mov_b32_e32 v45, v96
	v_add_f32_e32 v101, v0, v22
	v_mul_f32_e32 v0, v100, v100
	v_pk_add_f32 v[44:45], v[20:21], v[44:45]
	v_mov_b32_e32 v92, v26
	v_mul_f32_e32 v60, v101, v101
	v_pk_add_f32 v[48:49], v[26:27], v[92:93]
	v_pk_fma_f32 v[50:51], v[20:21], v[20:21], v[0:1]
	v_pk_mul_f32 v[52:53], v[44:45], v[44:45]
	v_pk_fma_f32 v[6:7], v[2:3], v[58:59], v[6:7] op_sel_hi:[0,1,1]
	v_pk_fma_f32 v[4:5], v[2:3], v[42:43], v[4:5] op_sel_hi:[0,1,1]
	v_mov_b32_e32 v51, v53
	v_pk_fma_f32 v[52:53], v[26:27], v[26:27], v[60:61]
	v_pk_mul_f32 v[54:55], v[48:49], v[48:49]
	v_pk_fma_f32 v[6:7], v[2:3], v[82:83], v[6:7] op_sel:[1,0,0]
	v_pk_fma_f32 v[4:5], v[2:3], v[84:85], v[4:5] op_sel:[1,0,0]
	v_mov_b32_e32 v53, v55
	v_pk_mul_f32 v[86:87], v[2:3], v[86:87] op_sel:[1,0] op_sel_hi:[0,1]
	v_pk_mul_f32 v[42:43], v[4:5], v[4:5]
	v_pk_add_f32 v[50:51], v[50:51], v[52:53]
	v_mov_b32_e32 v2, v6
	v_mov_b32_e32 v52, v6
	v_mov_b32_e32 v53, v94
	v_mul_f32_e32 v78, v7, v7
	v_mov_b32_e32 v54, v4
	v_mov_b32_e32 v55, v3
	v_mov_b32_e32 v58, v4
	v_mov_b32_e32 v59, v94
	v_pk_fma_f32 v[52:53], v[2:3], v[52:53], v[78:79]
	v_mov_b32_e32 v78, v43
	v_pk_fma_f32 v[42:43], v[54:55], v[58:59], v[78:79]
	v_pk_add_f32 v[54:55], v[52:53], v[42:43]
	v_pk_mul_f32 v[42:43], v[52:53], v[42:43]
	v_lshlrev_b32_e32 v0, 16, v1
	v_mov_b32_e32 v55, v43
	v_and_b32_e32 v1, 0xffff0000, v1
	v_mov_b32_e32 v42, v66
	v_mov_b32_e32 v43, v46
	v_pk_add_f32 v[0:1], v[42:43], v[0:1]
	v_mov_b32_e32 v46, v67
	v_pk_add_f32 v[0:1], v[0:1], v[46:47]
	v_mov_b32_e32 v42, v87
	v_mov_b32_e32 v43, v37
	v_pk_add_f32 v[0:1], v[0:1], v[42:43]
	v_mov_b32_e32 v87, v36
	v_pk_add_f32 v[36:37], v[0:1], v[86:87]
	v_mov_b32_e32 v27, v101
	v_pk_mul_f32 v[0:1], v[36:37], v[36:37]
	v_mov_b32_e32 v2, v37
	v_mov_b32_e32 v94, v37
	v_mov_b32_e32 v1, v41
	v_pk_fma_f32 v[0:1], v[2:3], v[94:95], v[0:1]
	v_lshl_add_u64 v[40:41], s[6:7], 0, v[8:9]
	v_pk_add_f32 v[2:3], v[38:39], v[0:1]
	v_pk_mul_f32 v[0:1], v[38:39], v[0:1]
	v_mov_b32_e32 v48, v45
	v_mov_b32_e32 v3, v1
	v_pk_add_f32 v[0:1], v[54:55], v[2:3]
	v_mov_b32_e32 v38, v53
	v_pk_add_f32 v[0:1], v[0:1], v[50:51]
	s_nop 0
	v_add_f32_e32 v0, v0, v1
	ds_bpermute_b32 v1, v28, v0
	s_waitcnt lgkmcnt(0)
	v_add_f32_e32 v0, v0, v1
	ds_bpermute_b32 v1, v29, v0
	s_waitcnt lgkmcnt(0)
	v_add_f32_e32 v0, v0, v1
	ds_bpermute_b32 v1, v30, v0
	s_waitcnt lgkmcnt(0)
	v_add_f32_e32 v0, v0, v1
	ds_bpermute_b32 v1, v31, v0
	s_waitcnt lgkmcnt(0)
	v_add_f32_e32 v0, v0, v1
	ds_bpermute_b32 v1, v32, v0
	s_waitcnt lgkmcnt(0)
	v_add_f32_e32 v0, v0, v1
	ds_bpermute_b32 v1, v33, v0
	s_waitcnt lgkmcnt(0)
	v_add_f32_e32 v0, v0, v1
	v_fmamk_f32 v0, v0, 0x3a800000, v34
	v_mul_f32_e32 v1, 0x4f800000, v0
	v_cmp_gt_f32_e32 vcc, s38, v0
	s_nop 1
	v_cndmask_b32_e32 v0, v0, v1, vcc
	v_sqrt_f32_e32 v1, v0
	s_nop 0
	v_add_u32_e32 v2, -1, v1
	v_fma_f32 v3, -v2, v1, v0
	v_cmp_ge_f32_e64 s[0:1], 0, v3
	v_add_u32_e32 v3, 1, v1
	s_nop 0
	v_cndmask_b32_e64 v2, v1, v2, s[0:1]
	v_fma_f32 v1, -v3, v1, v0
	v_cmp_lt_f32_e64 s[0:1], 0, v1
	s_nop 1
	v_cndmask_b32_e64 v1, v2, v3, s[0:1]
	v_mul_f32_e32 v2, 0x37800000, v1
	v_cndmask_b32_e32 v1, v1, v2, vcc
	v_cmp_class_f32_e32 vcc, v0, v35
	s_nop 1
	v_cndmask_b32_e32 v0, v1, v0, vcc
	v_div_scale_f32 v1, s[0:1], v0, v0, 1.0
	v_rcp_f32_e32 v2, v1
	s_nop 0
	v_fma_f32 v3, -v1, v2, 1.0
	v_fmac_f32_e32 v2, v3, v2
	v_div_scale_f32 v3, vcc, 1.0, v0, 1.0
	v_mul_f32_e32 v19, v3, v2
	v_fma_f32 v21, -v1, v19, v3
	v_fmac_f32_e32 v19, v21, v2
	v_fma_f32 v1, -v1, v19, v3
	v_div_fmas_f32 v1, v1, v2, v19
	v_div_fixup_f32 v42, v1, v0, 1.0
	v_pk_mul_f32 v[0:1], v[42:43], v[6:7] op_sel_hi:[0,1]
	v_pk_mul_f32 v[2:3], v[42:43], v[4:5] op_sel_hi:[0,1]
	s_waitcnt vmcnt(4)
	v_pk_mul_f32 v[2:3], v[202:203], v[2:3]
	v_pk_mul_f32 v[0:1], v[200:201], v[0:1]
	global_store_dwordx4 v[40:41], v[0:3], off
	v_mov_b32_e32 v19, v56
	v_pk_mul_f32 v[4:5], v[42:43], v[36:37] op_sel_hi:[0,1]
	v_pk_mul_f32 v[6:7], v[42:43], v[18:19] op_sel_hi:[0,1]
	v_mov_b32_e32 v21, v100
	v_pk_mul_f32 v[0:1], v[204:205], v[6:7]
	v_pk_mul_f32 v[2:3], v[206:207], v[4:5]
	global_store_dwordx4 v[40:41], v[0:3], off offset:1024
	v_pk_mul_f32 v[4:5], v[42:43], v[26:27] op_sel_hi:[0,1]
	v_pk_mul_f32 v[6:7], v[42:43], v[20:21] op_sel_hi:[0,1]
	v_pk_mul_f32 v[0:1], v[208:209], v[6:7]
	v_pk_mul_f32 v[2:3], v[210:211], v[4:5]
	global_store_dwordx4 v[40:41], v[0:3], off offset:2048
	v_pk_mul_f32 v[4:5], v[42:43], v[38:39] op_sel_hi:[0,1]
	v_pk_mul_f32 v[6:7], v[42:43], v[48:49] op_sel_hi:[0,1]
	v_pk_mul_f32 v[0:1], v[212:213], v[4:5]
	v_pk_mul_f32 v[2:3], v[214:215], v[6:7]
	global_store_dwordx4 v[40:41], v[0:3], off offset:3072
	s_branch .LBB0_1396
